# baseline (speedup 1.0000x reference)
.LBB2_18:
	s_or_b64 exec, exec, s[10:11]
	s_waitcnt vmcnt(0)
	s_or_b32 s4, s21, 1
	v_cmp_ne_u32_e32 vcc, s4, v107
	v_cmp_lt_u32_e64 s[4:5], 1, v96
	s_or_b64 s[4:5], s[4:5], vcc
	s_barrier
	s_and_saveexec_b64 s[10:11], s[4:5]
	s_xor_b64 s[4:5], exec, s[10:11]
	s_cbranch_execz .LBB2_25
	v_lshlrev_b32_e32 v1, 14, v107
	v_and_b32_e32 v1, 0xc000, v1
	v_add_u32_e32 v82, 0, v1
	v_add_u32_e32 v1, v82, v106
	ds_read_b128 v[34:37], v1
	ds_read_b128 v[50:53], v1 offset:4096
	v_add_u32_e32 v1, v82, v105
	s_mov_b32 s10, 0x3e38aa3b
	s_waitcnt lgkmcnt(0)
	v_mfma_f32_32x32x16_f16 v[34:49], v[34:37], v[78:81], 0
	v_mfma_f32_32x32x16_f16 v[50:65], v[50:53], v[78:81], 0
	ds_read_b128 v[78:81], v1
	ds_read_b128 v[84:87], v1 offset:4096
	v_add_u32_e32 v1, v82, v104
	s_waitcnt lgkmcnt(1)
	v_mfma_f32_32x32x16_f16 v[34:49], v[78:81], v[74:77], v[34:49]
	s_waitcnt lgkmcnt(0)
	v_mfma_f32_32x32x16_f16 v[50:65], v[84:87], v[74:77], v[50:65]
	ds_read_b128 v[74:77], v1
	ds_read_b128 v[78:81], v1 offset:4096
	v_add_u32_e32 v1, v82, v103
	v_lshlrev_b32_e32 v84, 2, v93
	v_mov_b32_e32 v85, 0xff800000
	s_waitcnt lgkmcnt(1)
	v_mfma_f32_32x32x16_f16 v[34:49], v[74:77], v[70:73], v[34:49]
	s_waitcnt lgkmcnt(0)
	v_mfma_f32_32x32x16_f16 v[50:65], v[78:81], v[70:73], v[50:65]
	ds_read_b128 v[70:73], v1 offset:4096
	s_waitcnt lgkmcnt(0)
	v_mfma_f32_32x32x16_f16 v[50:65], v[70:73], v[66:69], v[50:65]
	ds_read_b128 v[70:73], v1
	v_lshl_or_b32 v1, v107, 6, v84
	v_or_b32_e32 v74, 32, v1
	v_cmp_le_u32_e32 vcc, v74, v99
	s_nop 7
	v_cndmask_b32_e32 v80, v85, v50, vcc
	s_waitcnt lgkmcnt(0)
	v_mfma_f32_32x32x16_f16 v[34:49], v[70:73], v[66:69], v[34:49]
	v_cmp_le_u32_e32 vcc, v1, v99
	v_or_b32_e32 v50, 2, v1
	s_nop 9
	v_cndmask_b32_e32 v81, v85, v34, vcc
	v_cmp_lt_u32_e32 vcc, v1, v99
	s_nop 1
	v_cndmask_b32_e32 v34, v85, v35, vcc
	v_or_b32_e32 v35, 33, v1
	v_cmp_le_u32_e32 vcc, v35, v99
	s_nop 1
	v_cndmask_b32_e32 v35, v85, v51, vcc
	v_cmp_le_u32_e32 vcc, v50, v99
	v_or_b32_e32 v50, 34, v1
	v_mbcnt_hi_u32_b32 v51, -1, v101
	v_cndmask_b32_e32 v36, v85, v36, vcc
	v_cmp_le_u32_e32 vcc, v50, v99
	v_or_b32_e32 v50, 3, v1
	s_nop 0
	v_cndmask_b32_e32 v78, v85, v52, vcc
	v_cmp_le_u32_e32 vcc, v50, v99
	v_or_b32_e32 v50, 35, v1
	v_xor_b32_e32 v52, 32, v51
	v_cndmask_b32_e32 v37, v85, v37, vcc
	v_cmp_le_u32_e32 vcc, v50, v99
	v_or_b32_e32 v50, 8, v1
	s_nop 0
	v_cndmask_b32_e32 v79, v85, v53, vcc
	v_cmp_le_u32_e32 vcc, v50, v99
	s_nop 1
	v_cndmask_b32_e32 v74, v85, v38, vcc
	v_or_b32_e32 v38, 40, v1
	v_cmp_le_u32_e32 vcc, v38, v99
	v_or_b32_e32 v38, 9, v1
	s_nop 0
	v_cndmask_b32_e32 v75, v85, v54, vcc
	v_cmp_le_u32_e32 vcc, v38, v99
	v_or_b32_e32 v38, 41, v1
	s_nop 0
	v_cndmask_b32_e32 v76, v85, v39, vcc
	v_cmp_le_u32_e32 vcc, v38, v99
	v_or_b32_e32 v38, 10, v1
	v_or_b32_e32 v39, 48, v1
	v_cndmask_b32_e32 v77, v85, v55, vcc
	v_cmp_le_u32_e32 vcc, v38, v99
	v_or_b32_e32 v38, 42, v1
	s_nop 0
	v_cndmask_b32_e32 v70, v85, v40, vcc
	v_cmp_le_u32_e32 vcc, v38, v99
	v_or_b32_e32 v38, 11, v1
	v_or_b32_e32 v40, 17, v1
	v_cndmask_b32_e32 v71, v85, v56, vcc
	v_cmp_le_u32_e32 vcc, v38, v99
	v_or_b32_e32 v38, 43, v1
	s_nop 0
	v_cndmask_b32_e32 v72, v85, v41, vcc
	v_cmp_le_u32_e32 vcc, v38, v99
	v_or_b32_e32 v38, 16, v1
	s_nop 0
	v_cndmask_b32_e32 v73, v85, v57, vcc
	v_cmp_le_u32_e32 vcc, v38, v99
	s_nop 1
	v_cndmask_b32_e32 v38, v85, v42, vcc
	v_cmp_le_u32_e32 vcc, v39, v99
	s_nop 1
	v_cndmask_b32_e32 v39, v85, v58, vcc
	v_cmp_le_u32_e32 vcc, v40, v99
	v_or_b32_e32 v40, 49, v1
	s_nop 0
	v_cndmask_b32_e32 v68, v85, v43, vcc
	v_cmp_le_u32_e32 vcc, v40, v99
	v_or_b32_e32 v40, 18, v1
	s_nop 0
	v_cndmask_b32_e32 v69, v85, v59, vcc
	v_cmp_le_u32_e32 vcc, v40, v99
	v_or_b32_e32 v40, 50, v1
	s_nop 0
	v_cndmask_b32_e32 v42, v85, v44, vcc
	v_cmp_le_u32_e32 vcc, v40, v99
	v_or_b32_e32 v40, 19, v1
	s_nop 0
	v_cndmask_b32_e32 v43, v85, v60, vcc
	v_cmp_le_u32_e32 vcc, v40, v99
	v_or_b32_e32 v40, 51, v1
	s_nop 0
	v_cndmask_b32_e32 v66, v85, v45, vcc
	v_cmp_le_u32_e32 vcc, v40, v99
	v_or_b32_e32 v40, 24, v1
	s_nop 0
	v_cndmask_b32_e32 v67, v85, v61, vcc
	v_cmp_le_u32_e32 vcc, v40, v99
	v_or_b32_e32 v40, 56, v1
	s_nop 0
	v_cndmask_b32_e32 v58, v85, v46, vcc
	v_cmp_le_u32_e32 vcc, v40, v99
	v_or_b32_e32 v40, 25, v1
	s_nop 0
	v_cndmask_b32_e32 v59, v85, v62, vcc
	v_cmp_le_u32_e32 vcc, v40, v99
	v_or_b32_e32 v40, 57, v1
	s_nop 0
	v_cndmask_b32_e32 v60, v85, v47, vcc
	v_cmp_le_u32_e32 vcc, v40, v99
	v_or_b32_e32 v40, 26, v1
	s_nop 0
	v_cndmask_b32_e32 v61, v85, v63, vcc
	v_cmp_le_u32_e32 vcc, v40, v99
	v_or_b32_e32 v40, 58, v1
	s_nop 0
	v_cndmask_b32_e32 v57, v85, v48, vcc
	v_cmp_le_u32_e32 vcc, v40, v99
	v_or_b32_e32 v40, 27, v1
	v_or_b32_e32 v1, 59, v1
	v_cndmask_b32_e32 v55, v85, v64, vcc
	v_cmp_le_u32_e32 vcc, v40, v99
	v_max3_f32 v40, v80, v35, v78
	v_max3_f32 v40, v40, v79, v75
	v_cndmask_b32_e32 v56, v85, v49, vcc
	v_cmp_le_u32_e32 vcc, v1, v99
	v_max3_f32 v1, v81, v34, v36
	v_max3_f32 v1, v1, v37, v74
	v_max3_f32 v1, v1, v76, v70
	v_max3_f32 v40, v40, v77, v71
	v_max3_f32 v1, v1, v72, v38
	v_max3_f32 v40, v40, v73, v39
	v_cndmask_b32_e32 v54, v85, v65, vcc
	v_max3_f32 v1, v1, v68, v42
	v_max3_f32 v40, v40, v69, v43
	v_max3_f32 v1, v1, v66, v58
	v_max3_f32 v40, v40, v67, v59
	v_max_f32_e32 v41, v54, v54
	v_max_f32_e32 v44, v56, v56
	v_max3_f32 v1, v1, v60, v57
	v_max3_f32 v40, v40, v61, v55
	v_max_f32_e32 v41, v44, v41
	v_max3_f32 v1, v1, v40, v41
	v_and_b32_e32 v40, 64, v51
	v_add_u32_e32 v53, 64, v40
	v_cmp_lt_i32_e32 vcc, v52, v53
	s_nop 1
	v_mov_b32_e32 v40, v1
	s_nop 1
	v_permlane32_swap_b32_e32 v40, v1
	s_waitcnt lgkmcnt(0)
	v_max_f32_e32 v40, v1, v40
	v_fma_f32 v1, v40, s10, -v102
	s_mov_b32 s10, 0x41000000
	v_cmp_lt_f32_e32 vcc, s10, v1
	s_cbranch_vccz .LBB2_23
	v_mul_f32_e32 v1, 0x3e38aa3b, v40
	v_max_f32_e32 v1, v1, v1
	v_max_f32_e32 v40, v102, v102
	v_max_f32_e32 v50, v40, v1
	v_sub_f32_e32 v1, v102, v50
	v_exp_f32_e32 v40, v1
	v_cmp_gt_u32_e32 vcc, 32, v94
	s_and_saveexec_b64 s[10:11], vcc
	v_lshl_add_u32 v1, v95, 2, v100
	ds_write_b32 v1, v40
	s_or_b64 exec, exec, s[10:11]
	s_waitcnt lgkmcnt(0)
	v_lshl_add_u32 v1, v84, 2, v100
	ds_read_b128 v[44:47], v1 offset:96
	ds_read_b128 v[62:65], v1 offset:64
	ds_read_b128 v[84:87], v1 offset:32
	ds_read_b128 v[88:91], v1
	v_mul_f32_e32 v83, v83, v40
	s_waitcnt lgkmcnt(3)
	v_pk_mul_f32 v[32:33], v[32:33], v[46:47]
	s_waitcnt lgkmcnt(2)
	v_pk_mul_f32 v[28:29], v[28:29], v[64:65]
	s_waitcnt lgkmcnt(1)
	v_pk_mul_f32 v[24:25], v[24:25], v[86:87]
	s_waitcnt lgkmcnt(0)
	v_pk_mul_f32 v[20:21], v[20:21], v[90:91]
	v_pk_mul_f32 v[30:31], v[30:31], v[44:45]
	v_pk_mul_f32 v[26:27], v[26:27], v[62:63]
	v_pk_mul_f32 v[22:23], v[22:23], v[84:85]
	v_pk_mul_f32 v[18:19], v[18:19], v[88:89]
	v_pk_mul_f32 v[16:17], v[16:17], v[46:47]
	v_pk_mul_f32 v[12:13], v[12:13], v[64:65]
	v_pk_mul_f32 v[8:9], v[8:9], v[86:87]
	v_pk_mul_f32 v[4:5], v[4:5], v[90:91]
	v_pk_mul_f32 v[14:15], v[14:15], v[44:45]
	v_pk_mul_f32 v[10:11], v[10:11], v[62:63]
	v_pk_mul_f32 v[6:7], v[6:7], v[84:85]
	v_pk_mul_f32 v[2:3], v[2:3], v[88:89]
	s_branch .LBB2_24

.LBB2_25:
	s_andn2_saveexec_b64 s[4:5], s[4:5]
	v_mbcnt_hi_u32_b32 v51, -1, v101
	v_and_b32_e32 v1, 64, v51
	v_xor_b32_e32 v52, 32, v51
	v_add_u32_e32 v53, 64, v1
	v_mov_b32_e32 v50, v102
	s_or_b64 exec, exec, s[4:5]
	v_cmp_lt_i32_e32 vcc, v52, v53
	s_waitcnt lgkmcnt(0)
	s_barrier
	s_movk_i32 s4, 0x2200
	v_mad_u32_u24 v34, v96, s4, 0
	v_mov_b32_e32 v1, v83
	v_mov_b32_e32 v35, v83
	v_cmp_ne_u32_e32 vcc, 0, v97
	s_nop 0
	v_permlane32_swap_b32_e32 v35, v1
	s_waitcnt lgkmcnt(0)
	v_add_f32_e32 v35, v35, v1
	s_and_saveexec_b64 s[4:5], vcc
	s_cbranch_execz .LBB2_31
	v_cmp_gt_u32_e32 vcc, 32, v94
	s_and_saveexec_b64 s[10:11], vcc
	v_lshl_add_u32 v1, v95, 2, v34
	ds_write2_b32 v1, v50, v35 offset1:32
	s_or_b64 exec, exec, s[10:11]
	v_lshl_add_u32 v1, v94, 2, v34
	ds_write2st64_b32 v1, v18, v19 offset0:2 offset1:3
	ds_write2st64_b32 v1, v2, v3 offset0:18 offset1:19
	ds_write2st64_b32 v1, v20, v21 offset0:4 offset1:5
	ds_write2st64_b32 v1, v4, v5 offset0:20 offset1:21
	ds_write2st64_b32 v1, v22, v23 offset0:6 offset1:7
	ds_write2st64_b32 v1, v6, v7 offset0:22 offset1:23
	ds_write2st64_b32 v1, v24, v25 offset0:8 offset1:9
	ds_write2st64_b32 v1, v8, v9 offset0:24 offset1:25
	ds_write2st64_b32 v1, v26, v27 offset0:10 offset1:11
	ds_write2st64_b32 v1, v10, v11 offset0:26 offset1:27
	ds_write2st64_b32 v1, v28, v29 offset0:12 offset1:13
	ds_write2st64_b32 v1, v12, v13 offset0:28 offset1:29
	ds_write2st64_b32 v1, v30, v31 offset0:14 offset1:15
	ds_write2st64_b32 v1, v14, v15 offset0:30 offset1:31
	ds_write2st64_b32 v1, v32, v33 offset0:16 offset1:17
	ds_write2st64_b32 v1, v16, v17 offset0:32 offset1:33
